# attention QK^T burst leads with six bare MFMAs after the barrier, the previous tile's VALU head fills the shadow of the remaining ten
# baseline (speedup 1.0000x reference)
.LBB0_3234:
	s_waitcnt vmcnt(0)
	ds_read_b128 v[178:181], v198 offset:49152
	ds_read_b128 v[216:219], v198 offset:57344
	ds_read_b128 v[228:231], v204 offset:49152
	ds_read_b128 v[232:235], v204 offset:57344
	ds_read_b128 v[238:241], v205 offset:49152
	ds_read_b128 v[242:245], v205 offset:57344
	ds_read_b128 v[250:253], v206 offset:49152
	s_waitcnt lgkmcnt(6)
	v_mfma_f32_32x32x16_bf16 v[114:129], v[178:181], v[174:177], 0
	ds_read_b128 v[178:181], v206 offset:57344
	s_waitcnt lgkmcnt(6)
	v_mfma_f32_32x32x16_bf16 v[98:113], v[216:219], v[174:177], 0
	ds_read_b128 v[216:219], v198 offset:49280
	s_waitcnt lgkmcnt(6)
	v_mfma_f32_32x32x16_bf16 v[114:129], v[228:231], v[170:173], v[114:129]
	ds_read_b128 v[228:231], v191 offset:4096
	s_waitcnt lgkmcnt(6)
	v_mfma_f32_32x32x16_bf16 v[98:113], v[232:235], v[170:173], v[98:113]
	ds_read_b128 v[232:235], v198 offset:57472
	s_waitcnt lgkmcnt(6)
	v_mfma_f32_32x32x16_bf16 v[114:129], v[238:241], v[166:169], v[114:129]
	ds_read_b128 v[238:241], v204 offset:49280
	s_waitcnt lgkmcnt(6)
	v_mfma_f32_32x32x16_bf16 v[98:113], v[242:245], v[166:169], v[98:113]
	ds_read_b128 v[242:245], v191 offset:5120
	s_waitcnt lgkmcnt(6)
	v_mfma_f32_32x32x16_bf16 v[114:129], v[250:253], v[162:165], v[114:129]
	ds_read_b128 v[250:253], v204 offset:57472
	v_add_f32_e32 v16, 0, v154
	v_add_f32_e32 v16, v158, v16
	v_add_f32_e32 v16, v155, v16
	v_add_f32_e32 v16, v159, v16
	v_add_f32_e32 v16, v156, v16
	v_add_f32_e32 v16, v160, v16
	v_add_f32_e32 v16, v157, v16
	s_waitcnt lgkmcnt(6)
	v_mfma_f32_32x32x16_bf16 v[98:113], v[178:181], v[162:165], v[98:113]
	ds_read_b128 v[178:181], v205 offset:49280
	v_add_f32_e32 v16, v161, v16
	v_add_f32_e32 v16, v146, v16
	v_add_f32_e32 v16, v150, v16
	v_add_f32_e32 v16, v147, v16
	v_add_f32_e32 v16, v151, v16
	v_exp_f32_e32 v2, v144
	v_add_f32_e32 v16, v148, v16
	s_waitcnt lgkmcnt(5)
	v_mfma_f32_32x32x16_bf16 v[114:129], v[216:219], v[228:231], v[114:129]
	ds_read_b128 v[216:219], v191 offset:6144
	v_exp_f32_e32 v4, v145
	v_add_f32_e32 v16, v152, v16
	v_exp_f32_e32 v5, v140
	v_add_f32_e32 v16, v149, v16
	v_exp_f32_e32 v6, v141
	v_add_f32_e32 v16, v153, v16
	v_exp_f32_e32 v7, v138
	s_waitcnt lgkmcnt(5)
	v_mfma_f32_32x32x16_bf16 v[98:113], v[232:235], v[228:231], v[98:113]
	ds_read_b128 v[232:235], v205 offset:57472
	ds_read_b128 v[228:231], v206 offset:49280
	v_add_f32_e32 v16, v2, v16
	v_exp_f32_e32 v8, v139
	v_add_f32_e32 v16, v4, v16
	v_exp_f32_e32 v9, v132
	v_add_f32_e32 v16, v5, v16
	v_exp_f32_e32 v10, v133
	v_add_f32_e32 v16, v6, v16
	s_waitcnt lgkmcnt(5)
	v_mfma_f32_32x32x16_bf16 v[114:129], v[238:241], v[242:245], v[114:129]
	ds_read_b128 v[238:241], v191 offset:7168
	v_exp_f32_e32 v11, v130
	v_add_f32_e32 v16, v7, v16
	v_exp_f32_e32 v12, v131
	v_add_f32_e32 v16, v8, v16
	v_exp_f32_e32 v13, v142
	v_add_f32_e32 v16, v9, v16
	v_exp_f32_e32 v14, v143
	s_waitcnt lgkmcnt(5)
	v_mfma_f32_32x32x16_bf16 v[98:113], v[250:253], v[242:245], v[98:113]
	ds_read_b128 v[250:253], v206 offset:57472
	v_add_f32_e32 v16, v10, v16
	v_exp_f32_e32 v15, v136
	v_add_f32_e32 v16, v11, v16
	v_exp_f32_e32 v19, v137
	v_add_f32_e32 v16, v12, v16
	v_exp_f32_e32 v32, v134
	s_waitcnt lgkmcnt(4)
	v_mfma_f32_32x32x16_bf16 v[114:129], v[178:181], v[216:219], v[114:129]
	v_add_f32_e32 v16, v13, v16
	v_exp_f32_e32 v33, v135
	v_add_f32_e32 v16, v14, v16
	v_add_f32_e32 v16, v15, v16
	v_add_f32_e32 v16, v19, v16
	v_add_f32_e32 v16, v32, v16
	s_waitcnt lgkmcnt(3)
	v_mfma_f32_32x32x16_bf16 v[98:113], v[232:235], v[216:219], v[98:113]
	v_add_f32_e32 v16, v33, v16
	v_mov_b32_e32 v17, v16
	v_cvt_pk_bf16_f32 v20, v154, v158
	v_cvt_pk_bf16_f32 v21, v155, v159
	v_cvt_pk_bf16_f32 v22, v156, v160
	v_cvt_pk_bf16_f32 v23, v157, v161
	s_waitcnt lgkmcnt(1)
	v_mfma_f32_32x32x16_bf16 v[114:129], v[228:231], v[238:241], v[114:129]
	v_cvt_pk_bf16_f32 v24, v146, v150
	v_cvt_pk_bf16_f32 v25, v147, v151
	v_cvt_pk_bf16_f32 v26, v148, v152
	v_cvt_pk_bf16_f32 v27, v149, v153
	v_cvt_pk_bf16_f32 v28, v2, v4
	v_cvt_pk_bf16_f32 v29, v5, v6
	s_waitcnt lgkmcnt(0)
	v_mfma_f32_32x32x16_bf16 v[98:113], v[250:253], v[238:241], v[98:113]
	v_cvt_pk_bf16_f32 v30, v7, v8
	v_cvt_pk_bf16_f32 v31, v9, v10
	v_cvt_pk_bf16_f32 v130, v11, v12
	v_cvt_pk_bf16_f32 v131, v13, v14
	v_cvt_pk_bf16_f32 v132, v15, v19
	v_cvt_pk_bf16_f32 v133, v32, v33
	s_branch .LBB0_3238

.LBB0_3264:
	ds_read_b128 v[218:221], v198 offset:32768
	ds_read_b128 v[228:231], v198 offset:40960
	ds_read_b128 v[232:235], v204 offset:32768
	ds_read_b128 v[236:239], v204 offset:40960
	ds_read_b128 v[240:243], v205 offset:32768
	ds_read_b128 v[244:247], v205 offset:40960
	ds_read_b128 v[250:253], v206 offset:32768
	s_waitcnt lgkmcnt(6)
	v_mfma_f32_32x32x16_bf16 v[114:129], v[218:221], v[174:177], 0
	ds_read_b128 v[218:221], v206 offset:40960
	s_waitcnt lgkmcnt(6)
	v_mfma_f32_32x32x16_bf16 v[98:113], v[228:231], v[174:177], 0
	ds_read_b128 v[228:231], v198 offset:32896
	s_waitcnt lgkmcnt(6)
	v_mfma_f32_32x32x16_bf16 v[114:129], v[232:235], v[170:173], v[114:129]
	ds_read_b128 v[232:235], v191 offset:4096
	s_waitcnt lgkmcnt(6)
	v_mfma_f32_32x32x16_bf16 v[98:113], v[236:239], v[170:173], v[98:113]
	ds_read_b128 v[236:239], v198 offset:41088
	s_waitcnt lgkmcnt(6)
	v_mfma_f32_32x32x16_bf16 v[114:129], v[240:243], v[166:169], v[114:129]
	ds_read_b128 v[240:243], v204 offset:32896
	s_waitcnt lgkmcnt(6)
	v_mfma_f32_32x32x16_bf16 v[98:113], v[244:247], v[166:169], v[98:113]
	ds_read_b128 v[244:247], v191 offset:5120
	s_waitcnt lgkmcnt(6)
	v_mfma_f32_32x32x16_bf16 v[114:129], v[250:253], v[162:165], v[114:129]
	ds_read_b128 v[250:253], v204 offset:41088
	v_add_f32_e32 v19, 0, v142
	v_add_f32_e32 v19, v144, v19
	v_add_f32_e32 v19, v140, v19
	v_add_f32_e32 v19, v143, v19
	v_add_f32_e32 v19, v138, v19
	v_add_f32_e32 v19, v141, v19
	v_add_f32_e32 v19, v137, v19
	s_waitcnt lgkmcnt(6)
	v_mfma_f32_32x32x16_bf16 v[98:113], v[218:221], v[162:165], v[98:113]
	ds_read_b128 v[218:221], v205 offset:32896
	v_add_f32_e32 v19, v139, v19
	v_add_f32_e32 v19, v134, v19
	v_add_f32_e32 v19, v136, v19
	v_add_f32_e32 v19, v132, v19
	v_add_f32_e32 v19, v135, v19
	v_exp_f32_e32 v28, v146
	v_add_f32_e32 v19, v130, v19
	s_waitcnt lgkmcnt(5)
	v_mfma_f32_32x32x16_bf16 v[114:129], v[228:231], v[232:235], v[114:129]
	ds_read_b128 v[228:231], v191 offset:6144
	v_exp_f32_e32 v29, v147
	v_add_f32_e32 v19, v133, v19
	v_exp_f32_e32 v30, v148
	v_add_f32_e32 v19, v2, v19
	v_exp_f32_e32 v31, v149
	v_add_f32_e32 v19, v131, v19
	v_exp_f32_e32 v33, v150
	s_waitcnt lgkmcnt(5)
	v_mfma_f32_32x32x16_bf16 v[98:113], v[236:239], v[232:235], v[98:113]
	ds_read_b128 v[236:239], v205 offset:41088
	ds_read_b128 v[232:235], v206 offset:32896
	v_add_f32_e32 v19, v28, v19
	v_exp_f32_e32 v146, v151
	v_add_f32_e32 v19, v29, v19
	v_exp_f32_e32 v147, v152
	v_add_f32_e32 v19, v30, v19
	v_exp_f32_e32 v148, v153
	v_add_f32_e32 v19, v31, v19
	s_waitcnt lgkmcnt(5)
	v_mfma_f32_32x32x16_bf16 v[114:129], v[240:243], v[244:247], v[114:129]
	ds_read_b128 v[240:243], v191 offset:7168
	v_exp_f32_e32 v149, v154
	v_add_f32_e32 v19, v33, v19
	v_exp_f32_e32 v150, v155
	v_add_f32_e32 v19, v146, v19
	v_exp_f32_e32 v151, v156
	v_add_f32_e32 v19, v147, v19
	v_exp_f32_e32 v152, v157
	s_waitcnt lgkmcnt(5)
	v_mfma_f32_32x32x16_bf16 v[98:113], v[250:253], v[244:247], v[98:113]
	ds_read_b128 v[250:253], v206 offset:41088
	v_add_f32_e32 v19, v148, v19
	v_exp_f32_e32 v153, v158
	v_add_f32_e32 v19, v149, v19
	v_exp_f32_e32 v154, v159
	v_add_f32_e32 v19, v150, v19
	v_exp_f32_e32 v155, v160
	s_waitcnt lgkmcnt(4)
	v_mfma_f32_32x32x16_bf16 v[114:129], v[218:221], v[228:231], v[114:129]
	v_add_f32_e32 v19, v151, v19
	v_exp_f32_e32 v145, v145
	v_add_f32_e32 v19, v152, v19
	v_add_f32_e32 v19, v153, v19
	v_add_f32_e32 v19, v154, v19
	v_add_f32_e32 v19, v155, v19
	s_waitcnt lgkmcnt(3)
	v_mfma_f32_32x32x16_bf16 v[98:113], v[236:239], v[228:231], v[98:113]
	v_add_f32_e32 v19, v145, v19
	v_mov_b32_e32 v32, v19
	v_cvt_pk_bf16_f32 v20, v142, v144
	v_cvt_pk_bf16_f32 v21, v140, v143
	v_cvt_pk_bf16_f32 v22, v138, v141
	v_cvt_pk_bf16_f32 v23, v137, v139
	s_waitcnt lgkmcnt(1)
	v_mfma_f32_32x32x16_bf16 v[114:129], v[232:235], v[240:243], v[114:129]
	v_cvt_pk_bf16_f32 v24, v134, v136
	v_cvt_pk_bf16_f32 v25, v132, v135
	v_cvt_pk_bf16_f32 v26, v130, v133
	v_cvt_pk_bf16_f32 v27, v2, v131
	v_cvt_pk_bf16_f32 v28, v28, v29
	v_cvt_pk_bf16_f32 v29, v30, v31
	s_waitcnt lgkmcnt(0)
	v_mfma_f32_32x32x16_bf16 v[98:113], v[250:253], v[240:243], v[98:113]
	v_cvt_pk_bf16_f32 v30, v33, v146
	v_cvt_pk_bf16_f32 v31, v147, v148
	v_cvt_pk_bf16_f32 v130, v149, v150
	v_cvt_pk_bf16_f32 v131, v151, v152
	v_cvt_pk_bf16_f32 v132, v153, v154
	v_cvt_pk_bf16_f32 v133, v155, v145
	s_branch .LBB0_3268
